# norm1 row loop: all loads of a row (x, the four expert-output rows, g5; then g/shift/scale) issued up front with counted waits instead of one load/wait round trip per column group; plus previous chang
# speedup vs baseline: 1.0074x; 1.0074x over previous
; __device__ __forceinline__ unsigned cvt_pk_bf16(float lo, float hi) { unsigned r; asm volatile("v_cvt_pk_bf16_f32 %0, %1, %2" : "=v"(r) : "v"(lo), "v"(hi)); return r; }
;     __device__ __forceinline__ bf16_t* H() const { return (bf16_t*)(ws + WS_H); }
; __device__ __forceinline__ void phase_norm1(const Frame& F, const Params& P, int l, const float* xs, long long dctx, bool combine, float* xw, long long dctxw) {
;     ...
; #pragma unroll
;         for (int j = 0; j < 4; ++j) ss += v[j][0] * v[j][0] + v[j][1] * v[j][1] + v[j][2] * v[j][2] + v[j][3] * v[j][3];
;         ss = wave_sum(ss);
;         const float rstd = rsqrtf(ss * (1.f / 1024.f) + EPS);
; #pragma unroll
;         for (int j = 0; j < 4; ++j) {
;             const int col = F.lane * 4 + 256 * j;
;             const f32x4 gg = *(const f32x4*)(g + col), sh = *(const f32x4*)(md + col), sc = *(const f32x4*)(md + 1024 + col);
;             float o[4];
; #pragma unroll
;             for (int i = 0; i < 4; ++i) o[i] = v[j][i] * rstd * gg[i] * (1.f + sc[i]) + sh[i];
;             u32x2 w; w.x = cvt_pk_bf16(o[0], o[1]); w.y = cvt_pk_bf16(o[2], o[3]);
;             *(u32x2*)(F.H() + (size_t)row * DM + col) = w;
;         }
.LBB0_170:
	v_readlane_b32 s8, v255, 9
	s_mul_i32 s7, s8, 9
	s_add_i32 s2, s2, s7
	s_mul_hi_i32 s7, s2, 0x6000
	s_mulk_i32 s2, 0x6000
	s_add_u32 s18, s0, s2
	s_addc_u32 s19, s1, s7
	s_add_u32 s24, s18, 0x1000
	s_addc_u32 s25, s19, 0
	global_load_dwordx4 v[24:27], v[18:19], off
	global_load_dwordx4 v[32:35], v30, s[18:19]
	global_load_dwordx4 v[36:39], v30, s[24:25]
	global_load_dwordx4 v[44:47], v[18:19], off offset:1024
	global_load_dwordx4 v[48:51], v30, s[18:19] offset:1024
	global_load_dwordx4 v[52:55], v1, s[24:25]
	global_load_dwordx4 v[56:59], v[18:19], off offset:2048
	global_load_dwordx4 v[60:63], v30, s[18:19] offset:2048
	global_load_dwordx4 v[64:67], v28, s[24:25]
	global_load_dwordx4 v[68:71], v[18:19], off offset:3072
	global_load_dwordx4 v[72:75], v30, s[18:19] offset:3072
	global_load_dwordx4 v[76:79], v29, s[24:25]
	s_waitcnt vmcnt(0)
	v_mul_f32_e32 v22, v15, v15
	v_mul_f32_e32 v23, v11, v11
	v_fmac_f32_e32 v22, v14, v14
	v_fmac_f32_e32 v23, v10, v10
	v_fmac_f32_e32 v22, v16, v16
	v_fmac_f32_e32 v23, v12, v12
	v_fmac_f32_e32 v22, v17, v17
	v_fmac_f32_e32 v23, v13, v13
	v_add_f32_e32 v22, v22, v23
	v_mul_f32_e32 v23, v7, v7
	v_fmac_f32_e32 v23, v6, v6
	v_fmac_f32_e32 v23, v8, v8
	v_fmac_f32_e32 v23, v9, v9
	v_add_f32_e32 v22, v23, v22
	v_mul_f32_e32 v23, v3, v3
	v_fmac_f32_e32 v23, v2, v2
	v_fmac_f32_e32 v23, v4, v4
	v_fmac_f32_e32 v23, v5, v5
	v_add_f32_e32 v22, v23, v22
	s_mov_b32 s2, 0x13f16000
	v_readlane_b32 s9, v255, 10
	v_add_f32_dpp v22, v22, v22 quad_perm:[1,0,3,2] row_mask:0xf bank_mask:0xf bound_ctrl:1
	v_readlane_b32 s8, v254, 44
	v_readlane_b32 s9, v254, 45
	v_add_f32_dpp v22, v22, v22 quad_perm:[2,3,0,1] row_mask:0xf bank_mask:0xf bound_ctrl:1
	s_add_i32 s44, s44, s8
	v_readlane_b32 s8, v254, 40
	v_add_f32_dpp v22, v22, v22 row_half_mirror row_mask:0xf bank_mask:0xf bound_ctrl:1
	v_readlane_b32 s9, v254, 41
	s_add_u32 s46, s46, s8
	v_add_f32_dpp v22, v22, v22 row_mirror row_mask:0xf bank_mask:0xf bound_ctrl:1
	v_mov_b32_e32 v23, v22
	s_nop 1
	v_permlane16_swap_b32_e32 v22, v23
	v_add_f32_e32 v22, v22, v23
	v_mov_b32_e32 v23, v22
	s_nop 1
	v_permlane32_swap_b32_e32 v22, v23
	v_add_f32_e32 v22, v22, v23
	v_fmamk_f32 v22, v22, 0x3a800000, v196
	v_cmp_gt_f32_e32 vcc, s3, v22
	v_mul_f32_e32 v23, 0x4b800000, v22
	s_addc_u32 s47, s47, s9
	v_cndmask_b32_e32 v22, v22, v23, vcc
	v_rsq_f32_e32 v22, v22
	v_readlane_b32 s8, v254, 42
	v_readlane_b32 s9, v254, 43
	v_mul_f32_e32 v23, 0x45800000, v22
	v_cndmask_b32_e32 v22, v22, v23, vcc
	v_mul_f32_e32 v14, v14, v22
	v_mul_f32_e32 v15, v15, v22
	v_mul_f32_e32 v16, v16, v22
	v_mul_f32_e32 v10, v10, v22
	v_mul_f32_e32 v11, v11, v22
	v_mul_f32_e32 v12, v12, v22
	v_mul_f32_e32 v13, v13, v22
	v_mul_f32_e32 v6, v6, v22
	v_mul_f32_e32 v7, v7, v22
	v_mul_f32_e32 v8, v8, v22
	v_mul_f32_e32 v9, v9, v22
	v_mul_f32_e32 v2, v2, v22
	v_mul_f32_e32 v3, v3, v22
	v_mul_f32_e32 v4, v4, v22
	v_mul_f32_e32 v5, v5, v22
	v_mul_f32_e32 v14, v24, v14
	v_mul_f32_e32 v15, v25, v15
	v_add_f32_e32 v23, 1.0, v36
	v_fma_f32 v14, v23, v14, v32
	v_add_f32_e32 v23, 1.0, v37
	v_fma_f32 v15, v23, v15, v33
	v_mul_f32_e32 v16, v26, v16
	v_add_f32_e32 v23, 1.0, v38
	v_fma_f32 v23, v23, v16, v34
	v_mul_f32_e32 v16, v17, v22
	v_mul_f32_e32 v16, v27, v16
	v_add_f32_e32 v17, 1.0, v39
	v_fmac_f32_e32 v35, v17, v16
	v_cvt_pk_bf16_f32 v16, v14, v15
	v_lshl_add_u64 v[14:15], s[48:49], 0, v[146:147]
	v_add_co_u32_e32 v14, vcc, s2, v14
	v_cvt_pk_bf16_f32 v17, v23, v35
	s_add_u32 s48, s48, s8
	s_nop 0
	v_addc_co_u32_e32 v15, vcc, 0, v15, vcc
	global_store_dwordx2 v[14:15], v[16:17], off offset:256
	s_addc_u32 s49, s49, s9
	v_readlane_b32 s8, v254, 46
	v_readlane_b32 s9, v254, 47
	s_add_u32 s50, s50, s8
	s_addc_u32 s51, s51, s9
	s_add_u32 s52, s52, s8
	s_addc_u32 s53, s53, s9
	s_cmp_lt_i32 s44, 0x10800
	v_mul_f32_e32 v10, v44, v10
	v_mul_f32_e32 v11, v45, v11
	v_add_f32_e32 v16, 1.0, v52
	v_fma_f32 v10, v16, v10, v48
	v_add_f32_e32 v16, 1.0, v53
	v_fma_f32 v11, v16, v11, v49
	v_mul_f32_e32 v12, v46, v12
	v_add_f32_e32 v16, 1.0, v54
	v_fma_f32 v12, v16, v12, v50
	v_mul_f32_e32 v13, v47, v13
	v_add_f32_e32 v16, 1.0, v55
	v_fmac_f32_e32 v51, v16, v13
	v_cvt_pk_bf16_f32 v10, v10, v11
	v_cvt_pk_bf16_f32 v11, v12, v51
	global_store_dwordx2 v[14:15], v[10:11], off offset:768
	s_nop 0
	v_mul_f32_e32 v6, v6, v56
	v_mul_f32_e32 v7, v7, v57
	v_add_f32_e32 v10, 1.0, v64
	v_fma_f32 v6, v6, v10, v60
	v_add_f32_e32 v10, 1.0, v65
	v_fma_f32 v7, v7, v10, v61
	v_mul_f32_e32 v8, v8, v58
	v_add_f32_e32 v10, 1.0, v66
	v_fma_f32 v8, v8, v10, v62
	v_mul_f32_e32 v9, v9, v59
	v_add_f32_e32 v10, 1.0, v67
	v_fmac_f32_e32 v63, v9, v10
	v_cvt_pk_bf16_f32 v6, v6, v7
	v_cvt_pk_bf16_f32 v7, v8, v63
	global_store_dwordx2 v[14:15], v[6:7], off offset:1280
	s_nop 0
	v_mul_f32_e32 v2, v2, v68
	v_mul_f32_e32 v3, v3, v69
	v_add_f32_e32 v6, 1.0, v76
	v_fma_f32 v2, v2, v6, v72
	v_add_f32_e32 v6, 1.0, v77
	v_fma_f32 v3, v3, v6, v73
	v_mul_f32_e32 v4, v4, v70
	v_add_f32_e32 v6, 1.0, v78
	v_fma_f32 v4, v4, v6, v74
	v_mul_f32_e32 v5, v5, v71
	v_add_f32_e32 v6, 1.0, v79
	v_fmac_f32_e32 v75, v5, v6
	v_cvt_pk_bf16_f32 v2, v2, v3
	v_cvt_pk_bf16_f32 v3, v4, v75
	global_store_dwordx2 v[14:15], v[2:3], off offset:1792
	s_cbranch_scc0 .LBB0_173
; __device__ __forceinline__ float bf_lo(unsigned w) { return __uint_as_float(w << 16); }
; __device__ __forceinline__ float bf_hi(unsigned w) { return __uint_as_float(w & 0xffff0000u); }
;     __device__ __forceinline__ float* mods() const { return (float*)(ws + WS_MODS); }
;     __device__ __forceinline__ bf16_t* Y() const { return (bf16_t*)(ws + WS_Y); }
; __device__ __forceinline__ void phase_norm1(const Frame& F, const Params& P, int l, const float* xs, long long dctx, bool combine, float* xw, long long dctxw) {
;     ...
;         f32x4 v[4]; float ss = 0.f;
; #pragma unroll
;         for (int j = 0; j < 4; ++j) v[j] = *(const f32x4*)(xr + F.lane * 4 + 256 * j);
;         if (combine) {
;             const float* g5 = F.mods() + (size_t)((l - 1) * 9 + b) * 6144 + 5 * 1024;
;             const bf16_t* yr = F.Y() + (size_t)row * 4 * DM;
;             float* xo = xw + (size_t)row * DM + (row >= TL ? dctxw : 0ll);
; #pragma unroll
;             for (int j = 0; j < 4; ++j) {
;                 const int col = F.lane * 4 + 256 * j;
;                 f32x4 s = (f32x4){0.f, 0.f, 0.f, 0.f};
; #pragma unroll
;                 for (int k = 0; k < 4; ++k) { const u32x2 w = __builtin_nontemporal_load((const u32x2*)(yr + (size_t)k * DM + col));     s[0] += bf_lo(w.x); s[1] += bf_hi(w.x); s[2] += bf_lo(w.y); s[3] += bf_hi(w.y); }
;                 v[j] += *(const f32x4*)(g5 + col) * s;
;                 *(f32x4*)(xo + col) = v[j];
;             }
;         }
.LBB0_171:
	s_cmp_gt_i32 s44, 0xffff
	s_cselect_b64 s[8:9], -1, 0
	s_and_b64 s[18:19], s[8:9], exec
	s_cselect_b32 s19, s43, 0
	s_cselect_b32 s18, s42, 0
	v_lshl_add_u64 v[2:3], s[52:53], 0, v[20:21]
	v_lshl_add_u64 v[2:3], s[18:19], 2, v[2:3]
	global_load_dwordx4 v[14:17], v[2:3], off
	global_load_dwordx4 v[10:13], v[2:3], off offset:1024
	global_load_dwordx4 v[6:9], v[2:3], off offset:2048
	s_nop 0
	global_load_dwordx4 v[2:5], v[2:3], off offset:3072
	s_min_i32 s2, s44, 0x10000
	s_andn2_b64 vcc, exec, s[40:41]
	s_ashr_i32 s2, s2, 13
	s_cbranch_vccnz .LBB0_170
	s_mul_i32 s18, s2, 0x6000
	s_mul_hi_i32 s7, s2, 0x6000
	s_add_u32 s18, s0, s18
	s_addc_u32 s7, s1, s7
	s_add_u32 s28, s18, 0x5000
	s_addc_u32 s29, s7, 0
	v_lshl_add_u64 v[22:23], s[46:47], 0, v[146:147]
	s_mov_b32 s7, 0x1c316000
	v_add_co_u32_e32 v24, vcc, s7, v22
	s_mov_b32 s7, 0x1c317000
	s_nop 0
	v_addc_co_u32_e32 v25, vcc, 0, v23, vcc
	global_load_dwordx2 v[32:33], v[24:25], off offset:256 nt
	global_load_dwordx2 v[34:35], v[24:25], off offset:2304 nt
	v_add_co_u32_e32 v26, vcc, s7, v22
	s_and_b64 s[8:9], s[8:9], exec
	s_nop 0
	v_addc_co_u32_e32 v27, vcc, 0, v23, vcc
	global_load_dwordx2 v[22:23], v[26:27], off offset:256 nt
	global_load_dwordx2 v[36:37], v[26:27], off offset:2304 nt
	global_load_dwordx4 v[80:83], v30, s[28:29]
	global_load_dwordx2 v[84:85], v[24:25], off offset:768 nt
	global_load_dwordx2 v[86:87], v[24:25], off offset:2816 nt
	global_load_dwordx2 v[88:89], v[26:27], off offset:768 nt
	global_load_dwordx2 v[90:91], v[26:27], off offset:2816 nt
	global_load_dwordx4 v[92:95], v1, s[28:29]
	global_load_dwordx2 v[96:97], v[24:25], off offset:1280 nt
	global_load_dwordx2 v[98:99], v[24:25], off offset:3328 nt
	global_load_dwordx2 v[100:101], v[26:27], off offset:1280 nt
	global_load_dwordx2 v[102:103], v[26:27], off offset:3328 nt
	global_load_dwordx4 v[104:107], v28, s[28:29]
	global_load_dwordx2 v[108:109], v[24:25], off offset:1792 nt
	global_load_dwordx2 v[110:111], v[24:25], off offset:3840 nt
	global_load_dwordx2 v[112:113], v[26:27], off offset:1792 nt
	global_load_dwordx2 v[114:115], v[26:27], off offset:3840 nt
	global_load_dwordx4 v[116:119], v29, s[28:29]
	s_cselect_b32 s9, s61, 0
	s_cselect_b32 s8, s60, 0
	s_waitcnt vmcnt(15)
	v_lshlrev_b32_e32 v38, 16, v32
	v_and_b32_e32 v39, 0xffff0000, v32
	v_lshlrev_b32_e32 v32, 16, v33
	v_and_b32_e32 v33, 0xffff0000, v33
	v_pk_add_f32 v[38:39], v[38:39], 0 op_sel_hi:[1,0]
	v_lshlrev_b32_e32 v40, 16, v34
	v_and_b32_e32 v41, 0xffff0000, v34
	v_pk_add_f32 v[32:33], v[32:33], 0 op_sel_hi:[1,0]
	v_lshlrev_b32_e32 v34, 16, v35
	v_and_b32_e32 v35, 0xffff0000, v35
	v_pk_add_f32 v[38:39], v[38:39], v[40:41]
	v_lshlrev_b32_e32 v40, 16, v22
	v_and_b32_e32 v41, 0xffff0000, v22
	v_pk_add_f32 v[32:33], v[32:33], v[34:35]
	v_lshlrev_b32_e32 v22, 16, v23
	v_and_b32_e32 v23, 0xffff0000, v23
	v_pk_add_f32 v[22:23], v[32:33], v[22:23]
	v_lshlrev_b32_e32 v32, 16, v37
	v_and_b32_e32 v33, 0xffff0000, v37
	v_pk_add_f32 v[22:23], v[22:23], v[32:33]
	v_pk_add_f32 v[38:39], v[38:39], v[40:41]
	v_lshlrev_b32_e32 v40, 16, v36
	v_and_b32_e32 v41, 0xffff0000, v36
	v_pk_add_f32 v[38:39], v[38:39], v[40:41]
	v_pk_fma_f32 v[16:17], v[82:83], v[22:23], v[16:17]
	v_lshl_add_u64 v[22:23], s[50:51], 0, v[20:21]
	v_pk_fma_f32 v[14:15], v[80:81], v[38:39], v[14:15]
	v_lshl_add_u64 v[22:23], s[8:9], 2, v[22:23]
	global_store_dwordx4 v[22:23], v[14:17], off
	s_waitcnt vmcnt(11)
	v_lshlrev_b32_e32 v40, 16, v84
	v_and_b32_e32 v41, 0xffff0000, v84
	v_lshlrev_b32_e32 v32, 16, v85
	v_and_b32_e32 v33, 0xffff0000, v85
	v_lshlrev_b32_e32 v42, 16, v86
	v_and_b32_e32 v43, 0xffff0000, v86
	v_pk_add_f32 v[32:33], v[32:33], 0 op_sel_hi:[1,0]
	v_lshlrev_b32_e32 v34, 16, v87
	v_and_b32_e32 v35, 0xffff0000, v87
	v_pk_add_f32 v[32:33], v[32:33], v[34:35]
	v_lshlrev_b32_e32 v34, 16, v89
	v_and_b32_e32 v35, 0xffff0000, v89
	v_pk_add_f32 v[40:41], v[40:41], 0 op_sel_hi:[1,0]
	v_pk_add_f32 v[32:33], v[32:33], v[34:35]
	v_lshlrev_b32_e32 v34, 16, v91
	v_and_b32_e32 v35, 0xffff0000, v91
	v_pk_add_f32 v[40:41], v[40:41], v[42:43]
	v_lshlrev_b32_e32 v42, 16, v88
	v_and_b32_e32 v43, 0xffff0000, v88
	v_pk_add_f32 v[36:37], v[32:33], v[34:35]
	v_pk_add_f32 v[40:41], v[40:41], v[42:43]
	v_lshlrev_b32_e32 v42, 16, v90
	v_and_b32_e32 v43, 0xffff0000, v90
	v_pk_add_f32 v[40:41], v[40:41], v[42:43]
	v_pk_fma_f32 v[12:13], v[94:95], v[36:37], v[12:13]
	v_pk_fma_f32 v[10:11], v[92:93], v[40:41], v[10:11]
	global_store_dwordx4 v[22:23], v[10:13], off offset:1024
	s_waitcnt vmcnt(7)
	v_lshlrev_b32_e32 v40, 16, v96
	v_and_b32_e32 v41, 0xffff0000, v96
	v_lshlrev_b32_e32 v32, 16, v97
	v_and_b32_e32 v33, 0xffff0000, v97
	v_lshlrev_b32_e32 v42, 16, v98
	v_and_b32_e32 v43, 0xffff0000, v98
	v_pk_add_f32 v[32:33], v[32:33], 0 op_sel_hi:[1,0]
	v_lshlrev_b32_e32 v34, 16, v99
	v_and_b32_e32 v35, 0xffff0000, v99
	v_pk_add_f32 v[32:33], v[32:33], v[34:35]
	v_lshlrev_b32_e32 v34, 16, v101
	v_and_b32_e32 v35, 0xffff0000, v101
	v_pk_add_f32 v[40:41], v[40:41], 0 op_sel_hi:[1,0]
	v_pk_add_f32 v[32:33], v[32:33], v[34:35]
	v_lshlrev_b32_e32 v34, 16, v103
	v_and_b32_e32 v35, 0xffff0000, v103
	v_pk_add_f32 v[40:41], v[40:41], v[42:43]
	v_lshlrev_b32_e32 v42, 16, v100
	v_and_b32_e32 v43, 0xffff0000, v100
	v_pk_add_f32 v[36:37], v[32:33], v[34:35]
	v_pk_add_f32 v[40:41], v[40:41], v[42:43]
	v_lshlrev_b32_e32 v42, 16, v102
	v_and_b32_e32 v43, 0xffff0000, v102
	v_pk_add_f32 v[40:41], v[40:41], v[42:43]
	v_pk_fma_f32 v[8:9], v[106:107], v[36:37], v[8:9]
	v_pk_fma_f32 v[6:7], v[104:105], v[40:41], v[6:7]
	global_store_dwordx4 v[22:23], v[6:9], off offset:2048
	s_nop 0
	s_nop 0
	s_nop 0
	s_waitcnt vmcnt(3)
	v_lshlrev_b32_e32 v36, 16, v108
	v_and_b32_e32 v37, 0xffff0000, v108
	v_lshlrev_b32_e32 v32, 16, v109
	v_and_b32_e32 v33, 0xffff0000, v109
	v_pk_add_f32 v[36:37], v[36:37], 0 op_sel_hi:[1,0]
	v_lshlrev_b32_e32 v38, 16, v110
	v_and_b32_e32 v39, 0xffff0000, v110
	v_pk_add_f32 v[32:33], v[32:33], 0 op_sel_hi:[1,0]
	v_lshlrev_b32_e32 v24, 16, v111
	v_and_b32_e32 v25, 0xffff0000, v111
	v_pk_add_f32 v[36:37], v[36:37], v[38:39]
	v_lshlrev_b32_e32 v38, 16, v112
	v_and_b32_e32 v39, 0xffff0000, v112
	v_pk_add_f32 v[24:25], v[32:33], v[24:25]
	v_lshlrev_b32_e32 v32, 16, v113
	v_and_b32_e32 v33, 0xffff0000, v113
	v_pk_add_f32 v[36:37], v[36:37], v[38:39]
	v_lshlrev_b32_e32 v38, 16, v114
	v_and_b32_e32 v39, 0xffff0000, v114
	v_pk_add_f32 v[24:25], v[24:25], v[32:33]
	v_lshlrev_b32_e32 v26, 16, v115
	v_and_b32_e32 v27, 0xffff0000, v115
	v_pk_add_f32 v[32:33], v[24:25], v[26:27]
	v_pk_add_f32 v[36:37], v[36:37], v[38:39]
	v_pk_fma_f32 v[4:5], v[118:119], v[32:33], v[4:5]
	v_pk_fma_f32 v[2:3], v[116:117], v[36:37], v[2:3]
	global_store_dwordx4 v[22:23], v[2:5], off offset:3072
	s_branch .LBB0_170
